# speedup vs baseline: 1.0625x; 1.0056x over previous
_Z12final_kernelPKfS0_S0_S0_Pf:
	s_load_dwordx8 s[4:11], s[0:1], 0x0
	s_load_dwordx2 s[12:13], s[0:1], 0x20
	v_and_b32_e32 v1, 15, v0
	v_lshrrev_b32_e32 v2, 4, v0
	v_lshl_or_b32 v3, s2, 8, v0
	v_lshlrev_b32_e32 v3, 2, v3
	v_lshl_or_b32 v1, s2, 4, v1
	v_lshlrev_b32_e32 v1, 2, v1
	v_lshl_or_b32 v2, v2, 13, v1
	v_add_u32_e32 v4, 0x1000, v2
	s_mov_b32 s14, 0x800000
	s_mov_b32 s15, 0x3f317217
	s_mov_b32 s16, 0x7f800000
	v_mov_b32_e32 v18, 0x41b17218
	s_waitcnt lgkmcnt(0)
	global_load_dword v16, v3, s[4:5]
	global_load_dword v17, v3, s[6:7]
	global_load_dword v20, v2, s[8:9]
	global_load_dword v21, v2, s[8:9] offset:1024
	global_load_dword v22, v2, s[8:9] offset:2048
	global_load_dword v23, v2, s[8:9] offset:3072
	global_load_dword v24, v4, s[8:9]
	global_load_dword v25, v4, s[8:9] offset:1024
	global_load_dword v26, v4, s[8:9] offset:2048
	global_load_dword v27, v4, s[8:9] offset:3072
	global_load_dword v28, v2, s[10:11]
	global_load_dword v29, v2, s[10:11] offset:1024
	global_load_dword v30, v2, s[10:11] offset:2048
	global_load_dword v31, v2, s[10:11] offset:3072
	global_load_dword v32, v4, s[10:11]
	global_load_dword v33, v4, s[10:11] offset:1024
	global_load_dword v34, v4, s[10:11] offset:2048
	global_load_dword v35, v4, s[10:11] offset:3072
	v_lshrrev_b32_e32 v9, 6, v0
	v_lshlrev_b32_e32 v9, 2, v9
	v_and_b32_e32 v8, 15, v0
	v_lshl_add_u32 v8, v8, 4, v9
	s_waitcnt vmcnt(16)
	v_add_f32_e32 v14, v16, v17
	v_add_f32_e32 v14, 0x322bcc77, v14
	v_div_scale_f32 v15, s[18:19], v14, v14, v16
	v_rcp_f32_e32 v17, v15
	v_div_scale_f32 v19, vcc, v16, v14, v16
	v_fma_f32 v5, -v15, v17, 1.0
	v_fmac_f32_e32 v17, v5, v17
	v_mul_f32_e32 v5, v19, v17
	v_fma_f32 v6, -v15, v5, v19
	v_fmac_f32_e32 v5, v6, v17
	v_fma_f32 v15, -v15, v5, v19
	v_div_fmas_f32 v15, v15, v17, v5
	v_div_fixup_f32 v14, v15, v14, v16
	v_cmp_gt_f32_e32 vcc, s14, v14
	s_nop 1
	v_cndmask_b32_e64 v15, 0, 32, vcc
	v_ldexp_f32 v14, v14, v15
	v_log_f32_e32 v14, v14
	v_cndmask_b32_e32 v7, 0, v18, vcc
	v_mul_f32_e32 v15, 0x3f317217, v14
	v_fma_f32 v15, v14, s15, -v15
	v_fmamk_f32 v15, v14, 0x3377d1cf, v15
	v_fmac_f32_e32 v15, 0x3f317217, v14
	v_cmp_lt_f32_e64 vcc, |v14|, s16
	s_nop 1
	v_cndmask_b32_e32 v14, v14, v15, vcc
	v_sub_f32_e32 v14, v14, v7
	s_nop 1
	v_add_f32_dpp v14, v14, v14 quad_perm:[1,0,3,2] row_mask:0xf bank_mask:0xf bound_ctrl:1
	s_nop 1
	v_add_f32_dpp v14, v14, v14 quad_perm:[2,3,0,1] row_mask:0xf bank_mask:0xf bound_ctrl:1
	s_nop 1
	v_add_f32_dpp v14, v14, v14 row_half_mirror row_mask:0xf bank_mask:0xf bound_ctrl:1
	s_nop 1
	v_add_f32_dpp v14, v14, v14 row_mirror row_mask:0xf bank_mask:0xf bound_ctrl:1
	s_nop 1
	v_add_f32_dpp v14, v14, v14 row_bcast:15 row_mask:0xa bank_mask:0xf
	s_nop 1
	v_add_f32_dpp v14, v14, v14 row_bcast:31 row_mask:0xc bank_mask:0xf
	s_waitcnt vmcnt(8)
	v_add_f32_e32 v20, v20, v21
	v_add_f32_e32 v22, v22, v23
	v_add_f32_e32 v24, v24, v25
	v_add_f32_e32 v26, v26, v27
	v_add_f32_e32 v20, v20, v22
	v_add_f32_e32 v24, v24, v26
	v_add_f32_e32 v20, v20, v24
	s_waitcnt vmcnt(0)
	v_add_f32_e32 v28, v28, v29
	v_add_f32_e32 v30, v30, v31
	v_add_f32_e32 v32, v32, v33
	v_add_f32_e32 v34, v34, v35
	v_add_f32_e32 v28, v28, v30
	v_add_f32_e32 v32, v32, v34
	v_add_f32_e32 v28, v28, v32
	v_mov_b32_e32 v21, v20
	v_mov_b32_e32 v29, v28
	s_nop 1
	v_permlane16_swap_b32_e32 v20, v21
	v_permlane16_swap_b32_e32 v28, v29
	s_nop 1
	v_add_f32_e32 v20, v20, v21
	v_add_f32_e32 v28, v28, v29
	v_mov_b32_e32 v21, v20
	v_mov_b32_e32 v29, v28
	s_nop 1
	v_permlane32_swap_b32_e32 v20, v21
	v_permlane32_swap_b32_e32 v28, v29
	s_nop 1
	v_add_f32_e32 v20, v20, v21
	v_add_f32_e32 v28, v28, v29
	s_brev_b64 exec, 1
	ds_write_b32 v9, v14
	s_mov_b64 exec, 0xffff
	ds_write_b32 v8, v20 offset:16
	ds_write_b32 v8, v28 offset:272
	s_mov_b64 exec, -1
	s_waitcnt lgkmcnt(0)
	s_barrier
	v_cmp_gt_u32_e32 vcc, 16, v0
	s_and_saveexec_b64 s[14:15], vcc
	s_cbranch_execz .Lfk_end
	v_lshlrev_b32_e32 v1, 4, v0
	v_mov_b32_e32 v2, 0
	ds_read_b128 v[4:7], v1 offset:16
	ds_read_b128 v[10:13], v1 offset:272
	ds_read_b128 v[20:23], v2
	s_cmp_eq_u32 s2, 0
	s_cselect_b32 s3, 0.5, 0
	s_waitcnt lgkmcnt(1)
	v_add_f32_e32 v4, v4, v5
	v_add_f32_e32 v6, v6, v7
	v_add_f32_e32 v10, v10, v11
	v_add_f32_e32 v12, v12, v13
	v_add_f32_e32 v4, v4, v6
	v_add_f32_e32 v10, v10, v12
	v_mul_f32_e32 v4, v4, v10
	s_nop 1
	v_add_f32_dpp v4, v4, v4 quad_perm:[1,0,3,2] row_mask:0xf bank_mask:0xf bound_ctrl:1
	s_nop 1
	v_add_f32_dpp v4, v4, v4 quad_perm:[2,3,0,1] row_mask:0xf bank_mask:0xf bound_ctrl:1
	s_nop 1
	v_add_f32_dpp v4, v4, v4 row_half_mirror row_mask:0xf bank_mask:0xf bound_ctrl:1
	s_nop 1
	v_add_f32_dpp v4, v4, v4 row_mirror row_mask:0xf bank_mask:0xf bound_ctrl:1
	s_nop 1
	s_waitcnt lgkmcnt(0)
	v_add_f32_e32 v20, v20, v21
	v_add_f32_e32 v22, v22, v23
	v_add_f32_e32 v20, v20, v22
	v_mul_f32_e32 v5, 0xb9800000, v20
	v_mul_f32_e32 v6, 0xb10df4e0, v4
	v_add_f32_e32 v5, v5, v6
	v_add_f32_e32 v5, s3, v5
	v_cmp_eq_u32_e32 vcc, 0, v0
	s_and_b64 exec, exec, vcc
	global_atomic_add_f32 v2, v5, s[12:13]

	.amdhsa_kernel _Z12final_kernelPKfS0_S0_S0_Pf
		.amdhsa_group_segment_fixed_size 2064
		.amdhsa_private_segment_fixed_size 0
		.amdhsa_kernarg_size 40
		.amdhsa_user_sgpr_count 2
		.amdhsa_user_sgpr_dispatch_ptr 0
		.amdhsa_user_sgpr_queue_ptr 0
		.amdhsa_user_sgpr_kernarg_segment_ptr 1
		.amdhsa_user_sgpr_dispatch_id 0
		.amdhsa_user_sgpr_kernarg_preload_length 0
		.amdhsa_user_sgpr_kernarg_preload_offset 0
		.amdhsa_user_sgpr_private_segment_size 0
		.amdhsa_uses_dynamic_stack 0
		.amdhsa_enable_private_segment 0
		.amdhsa_system_sgpr_workgroup_id_x 1
		.amdhsa_system_sgpr_workgroup_id_y 0
		.amdhsa_system_sgpr_workgroup_id_z 0
		.amdhsa_system_sgpr_workgroup_info 0
		.amdhsa_system_vgpr_workitem_id 0
		.amdhsa_next_free_vgpr 36
		.amdhsa_next_free_sgpr 20
		.amdhsa_accum_offset 36
		.amdhsa_reserve_vcc 1
		.amdhsa_float_round_mode_32 0
		.amdhsa_float_round_mode_16_64 0
		.amdhsa_float_denorm_mode_32 3
		.amdhsa_float_denorm_mode_16_64 3
		.amdhsa_dx10_clamp 1
		.amdhsa_ieee_mode 1
		.amdhsa_fp16_overflow 0
		.amdhsa_tg_split 0
		.amdhsa_exception_fp_ieee_invalid_op 0
		.amdhsa_exception_fp_denorm_src 0
		.amdhsa_exception_fp_ieee_div_zero 0
		.amdhsa_exception_fp_ieee_overflow 0
		.amdhsa_exception_fp_ieee_underflow 0
		.amdhsa_exception_fp_ieee_inexact 0
		.amdhsa_exception_int_div_zero 0
	.end_amdhsa_kernel

amdhsa.kernels:
  - .agpr_count:     0
    .args:
      - .actual_access:  read_only
        .address_space:  global
        .offset:         0
        .size:           8
        .value_kind:     global_buffer
      - .actual_access:  read_only
        .address_space:  global
        .offset:         8
        .size:           8
        .value_kind:     global_buffer
      - .actual_access:  read_only
        .address_space:  global
        .offset:         16
        .size:           8
        .value_kind:     global_buffer
      - .actual_access:  write_only
        .address_space:  global
        .offset:         24
        .size:           8
        .value_kind:     global_buffer
      - .actual_access:  write_only
        .address_space:  global
        .offset:         32
        .size:           8
        .value_kind:     global_buffer
      - .actual_access:  write_only
        .address_space:  global
        .offset:         40
        .size:           8
        .value_kind:     global_buffer
      - .actual_access:  write_only
        .address_space:  global
        .offset:         48
        .size:           8
        .value_kind:     global_buffer
      - .actual_access:  write_only
        .address_space:  global
        .offset:         56
        .size:           8
        .value_kind:     global_buffer
    .group_segment_fixed_size: 36864
    .kernarg_segment_align: 8
    .kernarg_segment_size: 64
    .language:       OpenCL C
    .language_version:
      - 2
      - 0
    .max_flat_workgroup_size: 1024
    .name:           _Z11prep_kernelPKfS0_S0_PcPfS2_S2_S2_
    .private_segment_fixed_size: 0
    .sgpr_count:     38
    .sgpr_spill_count: 0
    .symbol:         _Z11prep_kernelPKfS0_S0_PcPfS2_S2_S2_.kd
    .uniform_work_group_size: 1
    .uses_dynamic_stack: false
    .vgpr_count:     64
    .vgpr_spill_count: 0
    .wavefront_size: 64
  - .agpr_count:     0
    .args:
      - .address_space:  global
        .offset:         0
        .size:           8
        .value_kind:     global_buffer
      - .address_space:  global
        .offset:         8
        .size:           8
        .value_kind:     global_buffer
      - .address_space:  global
        .offset:         16
        .size:           8
        .value_kind:     global_buffer
    .group_segment_fixed_size: 65536
    .kernarg_segment_align: 8
    .kernarg_segment_size: 24
    .language:       OpenCL C
    .language_version:
      - 2
      - 0
    .max_flat_workgroup_size: 512
    .name:           _Z11main_kernelPKcPfS1_
    .private_segment_fixed_size: 0
    .sgpr_count:     34
    .sgpr_spill_count: 0
    .symbol:         _Z11main_kernelPKcPfS1_.kd
    .uniform_work_group_size: 1
    .uses_dynamic_stack: false
    .vgpr_count:     128
    .vgpr_spill_count: 0
    .wavefront_size: 64
  - .agpr_count:     0
    .args:
      - .actual_access:  read_only
        .address_space:  global
        .offset:         0
        .size:           8
        .value_kind:     global_buffer
      - .actual_access:  read_only
        .address_space:  global
        .offset:         8
        .size:           8
        .value_kind:     global_buffer
      - .actual_access:  read_only
        .address_space:  global
        .offset:         16
        .size:           8
        .value_kind:     global_buffer
      - .actual_access:  read_only
        .address_space:  global
        .offset:         24
        .size:           8
        .value_kind:     global_buffer
      - .address_space:  global
        .offset:         32
        .size:           8
        .value_kind:     global_buffer
    .group_segment_fixed_size: 2064
    .kernarg_segment_align: 8
    .kernarg_segment_size: 40
    .language:       OpenCL C
    .language_version:
      - 2
      - 0
    .max_flat_workgroup_size: 256
    .name:           _Z12final_kernelPKfS0_S0_S0_Pf
    .private_segment_fixed_size: 0
    .sgpr_count:     26
    .sgpr_spill_count: 0
    .symbol:         _Z12final_kernelPKfS0_S0_S0_Pf.kd
    .uniform_work_group_size: 1
    .uses_dynamic_stack: false
    .vgpr_count:     36
    .vgpr_spill_count: 0
    .wavefront_size: 64
